# grid barrier release flattened: last XCD leader bumps all XCD generation words, other leaders wait on their own XCD word (one hop less); 10 loop barrier instances
# baseline (speedup 1.0000x reference)
.LBB0_263:
	s_or_b64 exec, exec, s[6:7]
	v_cvt_f32_u32_e32 v4, v2
	s_waitcnt vmcnt(0)
	v_readfirstlane_b32 s3, v3
	v_sub_u32_e32 v3, 0, v2
	v_rcp_iflag_f32_e32 v4, v4
	v_add_u32_e32 v5, s3, v1
	v_mul_f32_e32 v4, 0x4f7ffffe, v4
	v_cvt_u32_f32_e32 v4, v4
	v_mul_lo_u32 v1, v3, v4
	v_mul_hi_u32 v1, v4, v1
	v_add_u32_e32 v1, v4, v1
	v_mul_hi_u32 v1, v5, v1
	v_mul_lo_u32 v3, v1, v2
	v_sub_u32_e32 v3, v5, v3
	v_add_u32_e32 v4, 1, v1
	v_cmp_ge_u32_e32 vcc, v3, v2
	s_nop 1
	v_cndmask_b32_e32 v1, v1, v4, vcc
	v_sub_u32_e32 v4, v3, v2
	v_cndmask_b32_e32 v3, v3, v4, vcc
	v_add_u32_e32 v4, 1, v1
	v_cmp_ge_u32_e32 vcc, v3, v2
	v_add_u32_e32 v3, 1, v5
	s_nop 0
	v_cndmask_b32_e32 v1, v1, v4, vcc
	v_mul_lo_u32 v4, v2, v1
	v_add_u32_e32 v2, v4, v2
	v_cmp_ne_u32_e32 vcc, v3, v2
	v_readfirstlane_b32 s101, v1
	s_and_saveexec_b64 s[4:5], vcc
	s_xor_b64 s[4:5], exec, s[4:5]
	s_cbranch_execz .LBB0_277
	s_add_i32 s78, s2, 0x900
	s_lshl_b64 s[6:7], s[78:79], 2
	s_add_u32 s8, s82, s6
	s_addc_u32 s9, s83, s7
	s_waitcnt lgkmcnt(0)
	global_load_dword v0, v65, s[8:9] sc1
	s_waitcnt vmcnt(0)
	v_cmp_eq_u32_e32 vcc, v0, v1
	s_and_saveexec_b64 s[6:7], vcc
	s_cbranch_execz .LBB0_276
	s_mov_b32 s3, 1
	s_mov_b64 s[10:11], 0
	s_branch .LBB0_267

.LBB0_280:
	s_or_b64 exec, exec, s[6:7]
	s_waitcnt vmcnt(0)
	v_readfirstlane_b32 s3, v2
	v_cvt_f32_u32_e32 v2, v0
	v_sub_u32_e32 v3, 0, v0
	v_add_u32_e32 v1, s3, v1
	v_readlane_b32 s4, v243, 39
	v_rcp_iflag_f32_e32 v2, v2
	v_readlane_b32 s5, v243, 40
	s_mov_b64 s[6:7], -1
	v_mul_f32_e32 v2, 0x4f7ffffe, v2
	v_cvt_u32_f32_e32 v2, v2
	v_mul_lo_u32 v3, v3, v2
	v_mul_hi_u32 v3, v2, v3
	v_add_u32_e32 v2, v2, v3
	v_mul_hi_u32 v2, v1, v2
	v_mul_lo_u32 v3, v2, v0
	v_sub_u32_e32 v3, v1, v3
	v_cmp_ge_u32_e32 vcc, v3, v0
	v_add_u32_e32 v4, 1, v2
	v_add_u32_e32 v1, 1, v1
	v_cndmask_b32_e32 v2, v2, v4, vcc
	v_sub_u32_e32 v4, v3, v0
	v_cndmask_b32_e32 v3, v3, v4, vcc
	v_cmp_ge_u32_e32 vcc, v3, v0
	v_add_u32_e32 v3, 1, v2
	s_nop 0
	v_cndmask_b32_e32 v2, v2, v3, vcc
	v_mul_lo_u32 v3, v0, v2
	v_add_u32_e32 v0, v3, v0
	v_cmp_ne_u32_e32 vcc, v1, v0
	v_mov_b64_e32 v[0:1], s[4:5]
	s_mov_b32 s100, 1
	s_and_saveexec_b64 s[4:5], vcc
	s_cbranch_execz .LBB0_292
	s_mov_b32 s100, 0
	s_add_i32 s78, s2, 0x900
	s_lshl_b64 s[6:7], s[78:79], 2
	s_add_u32 s6, s82, s6
	s_addc_u32 s7, s83, s7
	s_mov_b64 s[8:9], 0
	s_nop 3
	global_load_dword v0, v65, s[6:7] sc1
	s_waitcnt vmcnt(0)
	v_mov_b32_e32 v2, s101
	v_cmp_eq_u32_e32 vcc, v0, v2
	s_and_saveexec_b64 s[6:7], vcc
	s_cbranch_execz .LBB0_291
	s_mov_b32 s3, 1
	s_branch .LBB0_284

.LBB0_286:
	s_add_i32 s78, s2, 0x900
	s_lshl_b64 s[12:13], s[78:79], 2
	s_add_u32 s12, s82, s12
	s_addc_u32 s13, s83, s13
	s_add_i32 s3, s3, 1
	s_mov_b64 s[14:15], -1
	s_nop 2
	global_load_dword v0, v65, s[12:13] sc1
	s_waitcnt vmcnt(0)
	v_cmp_ne_u32_e32 vcc, v0, v2
	s_orn2_b64 s[12:13], vcc, exec
	s_branch .LBB0_283

.LBB0_294:
	s_or_b64 exec, exec, s[4:5]
	s_mov_b64 s[4:5], exec
	v_mbcnt_lo_u32_b32 v0, s4, 0
	v_mbcnt_hi_u32_b32 v0, s5, v0
	v_cmp_eq_u32_e32 vcc, 0, v0
	s_waitcnt vmcnt(0)
	s_and_saveexec_b64 s[6:7], vcc
	s_cbranch_execz .LBB0_296
	s_cmp_eq_u32 s100, 0
	s_cbranch_scc1 .Lxb_relskip_0
	s_add_u32 s2, s82, 0x2400
	s_addc_u32 s3, s83, 0
	s_bcnt1_i32_b64 s4, s[4:5]
	v_mov_b32_e32 v0, s4
	global_atomic_add v65, v0, s[2:3]
	global_atomic_add v65, v0, s[2:3] offset:256
	global_atomic_add v65, v0, s[2:3] offset:512
	global_atomic_add v65, v0, s[2:3] offset:768
	global_atomic_add v65, v0, s[2:3] offset:1024
	global_atomic_add v65, v0, s[2:3] offset:1280
	global_atomic_add v65, v0, s[2:3] offset:1536
	global_atomic_add v65, v0, s[2:3] offset:1792
	global_atomic_add v65, v0, s[2:3] offset:2048
	global_atomic_add v65, v0, s[2:3] offset:2304
	global_atomic_add v65, v0, s[2:3] offset:2560
	global_atomic_add v65, v0, s[2:3] offset:2816
	global_atomic_add v65, v0, s[2:3] offset:3072
	global_atomic_add v65, v0, s[2:3] offset:3328
	global_atomic_add v65, v0, s[2:3] offset:3584
	global_atomic_add v65, v0, s[2:3] offset:3840
.Lxb_relskip_0:
.LBB0_296:
	s_or_b64 exec, exec, s[6:7]
	s_waitcnt vmcnt(0)

.LBB0_600:
	s_or_b64 exec, exec, s[8:9]
	v_cvt_f32_u32_e32 v4, v2
	s_waitcnt vmcnt(0)
	v_readfirstlane_b32 s1, v3
	v_sub_u32_e32 v3, 0, v2
	v_rcp_iflag_f32_e32 v4, v4
	v_add_u32_e32 v5, s1, v1
	v_mul_f32_e32 v4, 0x4f7ffffe, v4
	v_cvt_u32_f32_e32 v4, v4
	v_mul_lo_u32 v1, v3, v4
	v_mul_hi_u32 v1, v4, v1
	v_add_u32_e32 v1, v4, v1
	v_mul_hi_u32 v1, v5, v1
	v_mul_lo_u32 v3, v1, v2
	v_sub_u32_e32 v3, v5, v3
	v_add_u32_e32 v4, 1, v1
	v_cmp_ge_u32_e32 vcc, v3, v2
	s_nop 1
	v_cndmask_b32_e32 v1, v1, v4, vcc
	v_sub_u32_e32 v4, v3, v2
	v_cndmask_b32_e32 v3, v3, v4, vcc
	v_add_u32_e32 v4, 1, v1
	v_cmp_ge_u32_e32 vcc, v3, v2
	v_add_u32_e32 v3, 1, v5
	s_nop 0
	v_cndmask_b32_e32 v1, v1, v4, vcc
	v_mul_lo_u32 v4, v2, v1
	v_add_u32_e32 v2, v4, v2
	v_cmp_ne_u32_e32 vcc, v3, v2
	v_readfirstlane_b32 s101, v1
	s_and_saveexec_b64 s[2:3], vcc
	s_xor_b64 s[6:7], exec, s[2:3]
	s_cbranch_execz .LBB0_614
	s_add_i32 s78, s0, 0x900
	s_lshl_b64 s[2:3], s[78:79], 2
	s_add_u32 s10, s82, s2
	s_addc_u32 s11, s83, s3
	s_waitcnt lgkmcnt(0)
	global_load_dword v0, v65, s[10:11] sc1
	s_waitcnt vmcnt(0)
	v_cmp_eq_u32_e32 vcc, v0, v1
	s_and_saveexec_b64 s[8:9], vcc
	s_cbranch_execz .LBB0_613
	s_mov_b32 s1, 1
	s_mov_b64 s[12:13], 0
	s_branch .LBB0_604

.LBB0_617:
	s_or_b64 exec, exec, s[8:9]
	s_waitcnt vmcnt(0)
	v_readfirstlane_b32 s1, v2
	v_cvt_f32_u32_e32 v2, v0
	v_sub_u32_e32 v3, 0, v0
	v_add_u32_e32 v1, s1, v1
	v_readlane_b32 s2, v243, 39
	v_rcp_iflag_f32_e32 v2, v2
	v_readlane_b32 s3, v243, 40
	s_mov_b64 s[8:9], -1
	v_mul_f32_e32 v2, 0x4f7ffffe, v2
	v_cvt_u32_f32_e32 v2, v2
	v_mul_lo_u32 v3, v3, v2
	v_mul_hi_u32 v3, v2, v3
	v_add_u32_e32 v2, v2, v3
	v_mul_hi_u32 v2, v1, v2
	v_mul_lo_u32 v3, v2, v0
	v_sub_u32_e32 v3, v1, v3
	v_cmp_ge_u32_e32 vcc, v3, v0
	v_add_u32_e32 v4, 1, v2
	v_add_u32_e32 v1, 1, v1
	v_cndmask_b32_e32 v2, v2, v4, vcc
	v_sub_u32_e32 v4, v3, v0
	v_cndmask_b32_e32 v3, v3, v4, vcc
	v_cmp_ge_u32_e32 vcc, v3, v0
	v_add_u32_e32 v3, 1, v2
	s_nop 0
	v_cndmask_b32_e32 v2, v2, v3, vcc
	v_mul_lo_u32 v3, v0, v2
	v_add_u32_e32 v0, v3, v0
	v_cmp_ne_u32_e32 vcc, v1, v0
	v_mov_b64_e32 v[0:1], s[2:3]
	s_mov_b32 s100, 1
	s_and_saveexec_b64 s[6:7], vcc
	s_cbranch_execz .LBB0_629
	s_mov_b32 s100, 0
	s_add_i32 s78, s0, 0x900
	s_lshl_b64 s[2:3], s[78:79], 2
	s_add_u32 s2, s82, s2
	s_addc_u32 s3, s83, s3
	s_mov_b64 s[10:11], 0
	s_nop 3
	global_load_dword v0, v65, s[2:3] sc1
	s_waitcnt vmcnt(0)
	v_mov_b32_e32 v2, s101
	v_cmp_eq_u32_e32 vcc, v0, v2
	s_and_saveexec_b64 s[8:9], vcc
	s_cbranch_execz .LBB0_628
	s_mov_b32 s1, 1
	s_branch .LBB0_621

.LBB0_623:
	s_add_i32 s78, s0, 0x900
	s_lshl_b64 s[2:3], s[78:79], 2
	s_add_u32 s2, s82, s2
	s_addc_u32 s3, s83, s3
	s_add_i32 s1, s1, 1
	s_mov_b64 s[16:17], -1
	s_nop 2
	global_load_dword v0, v65, s[2:3] sc1
	s_waitcnt vmcnt(0)
	v_cmp_ne_u32_e32 vcc, v0, v2
	s_orn2_b64 s[14:15], vcc, exec
	s_branch .LBB0_620

.LBB0_631:
	s_or_b64 exec, exec, s[6:7]
	s_mov_b64 s[6:7], exec
	v_mbcnt_lo_u32_b32 v0, s6, 0
	v_mbcnt_hi_u32_b32 v0, s7, v0
	v_cmp_eq_u32_e32 vcc, 0, v0
	s_waitcnt vmcnt(0)
	s_and_saveexec_b64 s[8:9], vcc
	s_cbranch_execz .LBB0_633
	s_cmp_eq_u32 s100, 0
	s_cbranch_scc1 .Lxb_relskip_2
	s_add_u32 s0, s82, 0x2400
	s_addc_u32 s1, s83, 0
	s_bcnt1_i32_b64 s2, s[6:7]
	v_mov_b32_e32 v0, s2
	global_atomic_add v65, v0, s[0:1]
	global_atomic_add v65, v0, s[0:1] offset:256
	global_atomic_add v65, v0, s[0:1] offset:512
	global_atomic_add v65, v0, s[0:1] offset:768
	global_atomic_add v65, v0, s[0:1] offset:1024
	global_atomic_add v65, v0, s[0:1] offset:1280
	global_atomic_add v65, v0, s[0:1] offset:1536
	global_atomic_add v65, v0, s[0:1] offset:1792
	global_atomic_add v65, v0, s[0:1] offset:2048
	global_atomic_add v65, v0, s[0:1] offset:2304
	global_atomic_add v65, v0, s[0:1] offset:2560
	global_atomic_add v65, v0, s[0:1] offset:2816
	global_atomic_add v65, v0, s[0:1] offset:3072
	global_atomic_add v65, v0, s[0:1] offset:3328
	global_atomic_add v65, v0, s[0:1] offset:3584
	global_atomic_add v65, v0, s[0:1] offset:3840
.Lxb_relskip_2:
.LBB0_633:
	s_or_b64 exec, exec, s[8:9]
	s_waitcnt vmcnt(0)

.LBB0_1015:
	s_or_b64 exec, exec, s[4:5]
	v_cvt_f32_u32_e32 v4, v2
	s_waitcnt vmcnt(0)
	v_readfirstlane_b32 s2, v3
	v_sub_u32_e32 v3, 0, v2
	v_rcp_iflag_f32_e32 v4, v4
	v_add_u32_e32 v5, s2, v1
	v_mul_f32_e32 v4, 0x4f7ffffe, v4
	v_cvt_u32_f32_e32 v4, v4
	v_mul_lo_u32 v1, v3, v4
	v_mul_hi_u32 v1, v4, v1
	v_add_u32_e32 v1, v4, v1
	v_mul_hi_u32 v1, v5, v1
	v_mul_lo_u32 v3, v1, v2
	v_sub_u32_e32 v3, v5, v3
	v_add_u32_e32 v4, 1, v1
	v_cmp_ge_u32_e32 vcc, v3, v2
	s_nop 1
	v_cndmask_b32_e32 v1, v1, v4, vcc
	v_sub_u32_e32 v4, v3, v2
	v_cndmask_b32_e32 v3, v3, v4, vcc
	v_add_u32_e32 v4, 1, v1
	v_cmp_ge_u32_e32 vcc, v3, v2
	v_add_u32_e32 v3, 1, v5
	s_nop 0
	v_cndmask_b32_e32 v1, v1, v4, vcc
	v_mul_lo_u32 v4, v2, v1
	v_add_u32_e32 v2, v4, v2
	v_cmp_ne_u32_e32 vcc, v3, v2
	v_readfirstlane_b32 s101, v1
	s_and_saveexec_b64 s[2:3], vcc
	s_xor_b64 s[2:3], exec, s[2:3]
	s_cbranch_execz .LBB0_1029
	s_add_i32 s78, s18, 0x900
	s_lshl_b64 s[4:5], s[78:79], 2
	s_add_u32 s6, s82, s4
	s_addc_u32 s7, s83, s5
	s_waitcnt lgkmcnt(0)
	global_load_dword v0, v65, s[6:7] sc1
	s_waitcnt vmcnt(0)
	v_cmp_eq_u32_e32 vcc, v0, v1
	s_and_saveexec_b64 s[4:5], vcc
	s_cbranch_execz .LBB0_1028
	s_mov_b32 s19, 1
	s_mov_b64 s[8:9], 0
	s_branch .LBB0_1019

.LBB0_1032:
	s_or_b64 exec, exec, s[4:5]
	s_waitcnt vmcnt(0)
	v_readfirstlane_b32 s2, v2
	v_cvt_f32_u32_e32 v2, v0
	v_sub_u32_e32 v3, 0, v0
	v_add_u32_e32 v1, s2, v1
	v_readlane_b32 s2, v243, 39
	v_rcp_iflag_f32_e32 v2, v2
	v_readlane_b32 s3, v243, 40
	s_mov_b64 s[4:5], -1
	v_mul_f32_e32 v2, 0x4f7ffffe, v2
	v_cvt_u32_f32_e32 v2, v2
	v_mul_lo_u32 v3, v3, v2
	v_mul_hi_u32 v3, v2, v3
	v_add_u32_e32 v2, v2, v3
	v_mul_hi_u32 v2, v1, v2
	v_mul_lo_u32 v3, v2, v0
	v_sub_u32_e32 v3, v1, v3
	v_cmp_ge_u32_e32 vcc, v3, v0
	v_add_u32_e32 v4, 1, v2
	v_add_u32_e32 v1, 1, v1
	v_cndmask_b32_e32 v2, v2, v4, vcc
	v_sub_u32_e32 v4, v3, v0
	v_cndmask_b32_e32 v3, v3, v4, vcc
	v_cmp_ge_u32_e32 vcc, v3, v0
	v_add_u32_e32 v3, 1, v2
	s_nop 0
	v_cndmask_b32_e32 v2, v2, v3, vcc
	v_mul_lo_u32 v3, v0, v2
	v_add_u32_e32 v0, v3, v0
	v_cmp_ne_u32_e32 vcc, v1, v0
	v_mov_b64_e32 v[0:1], s[2:3]
	s_mov_b32 s100, 1
	s_and_saveexec_b64 s[2:3], vcc
	s_cbranch_execz .LBB0_1044
	s_mov_b32 s100, 0
	s_add_i32 s78, s18, 0x900
	s_lshl_b64 s[4:5], s[78:79], 2
	s_add_u32 s4, s82, s4
	s_addc_u32 s5, s83, s5
	s_mov_b64 s[6:7], 0
	s_nop 3
	global_load_dword v0, v65, s[4:5] sc1
	s_waitcnt vmcnt(0)
	v_mov_b32_e32 v2, s101
	v_cmp_eq_u32_e32 vcc, v0, v2
	s_and_saveexec_b64 s[4:5], vcc
	s_cbranch_execz .LBB0_1043
	s_mov_b32 s16, 1
	s_branch .LBB0_1036

.LBB0_1038:
	s_add_i32 s78, s18, 0x900
	s_lshl_b64 s[10:11], s[78:79], 2
	s_add_u32 s10, s82, s10
	s_addc_u32 s11, s83, s11
	s_add_i32 s16, s16, 1
	s_mov_b64 s[12:13], -1
	s_nop 2
	global_load_dword v0, v65, s[10:11] sc1
	s_waitcnt vmcnt(0)
	v_cmp_ne_u32_e32 vcc, v0, v2
	s_orn2_b64 s[10:11], vcc, exec
	s_branch .LBB0_1035

.LBB0_1046:
	s_or_b64 exec, exec, s[2:3]
	s_mov_b64 s[2:3], exec
	v_mbcnt_lo_u32_b32 v0, s2, 0
	v_mbcnt_hi_u32_b32 v0, s3, v0
	v_cmp_eq_u32_e32 vcc, 0, v0
	s_waitcnt vmcnt(0)
	s_and_saveexec_b64 s[4:5], vcc
	s_cbranch_execz .LBB0_1048
	s_cmp_eq_u32 s100, 0
	s_cbranch_scc1 .Lxb_relskip_6
	s_add_u32 s6, s82, 0x2400
	s_addc_u32 s7, s83, 0
	s_bcnt1_i32_b64 s2, s[2:3]
	v_mov_b32_e32 v0, s2
	global_atomic_add v65, v0, s[6:7]
	global_atomic_add v65, v0, s[6:7] offset:256
	global_atomic_add v65, v0, s[6:7] offset:512
	global_atomic_add v65, v0, s[6:7] offset:768
	global_atomic_add v65, v0, s[6:7] offset:1024
	global_atomic_add v65, v0, s[6:7] offset:1280
	global_atomic_add v65, v0, s[6:7] offset:1536
	global_atomic_add v65, v0, s[6:7] offset:1792
	global_atomic_add v65, v0, s[6:7] offset:2048
	global_atomic_add v65, v0, s[6:7] offset:2304
	global_atomic_add v65, v0, s[6:7] offset:2560
	global_atomic_add v65, v0, s[6:7] offset:2816
	global_atomic_add v65, v0, s[6:7] offset:3072
	global_atomic_add v65, v0, s[6:7] offset:3328
	global_atomic_add v65, v0, s[6:7] offset:3584
	global_atomic_add v65, v0, s[6:7] offset:3840
.Lxb_relskip_6:
.LBB0_1048:
	s_or_b64 exec, exec, s[4:5]
	s_waitcnt vmcnt(0)

.LBB0_1432:
	s_or_b64 exec, exec, s[4:5]
	v_cvt_f32_u32_e32 v4, v2
	s_waitcnt vmcnt(0)
	v_readfirstlane_b32 s2, v3
	v_sub_u32_e32 v3, 0, v2
	v_rcp_iflag_f32_e32 v4, v4
	v_add_u32_e32 v5, s2, v1
	v_mul_f32_e32 v4, 0x4f7ffffe, v4
	v_cvt_u32_f32_e32 v4, v4
	v_mul_lo_u32 v1, v3, v4
	v_mul_hi_u32 v1, v4, v1
	v_add_u32_e32 v1, v4, v1
	v_mul_hi_u32 v1, v5, v1
	v_mul_lo_u32 v3, v1, v2
	v_sub_u32_e32 v3, v5, v3
	v_add_u32_e32 v4, 1, v1
	v_cmp_ge_u32_e32 vcc, v3, v2
	s_nop 1
	v_cndmask_b32_e32 v1, v1, v4, vcc
	v_sub_u32_e32 v4, v3, v2
	v_cndmask_b32_e32 v3, v3, v4, vcc
	v_add_u32_e32 v4, 1, v1
	v_cmp_ge_u32_e32 vcc, v3, v2
	v_add_u32_e32 v3, 1, v5
	s_nop 0
	v_cndmask_b32_e32 v1, v1, v4, vcc
	v_mul_lo_u32 v4, v2, v1
	v_add_u32_e32 v2, v4, v2
	v_cmp_ne_u32_e32 vcc, v3, v2
	v_readfirstlane_b32 s101, v1
	s_and_saveexec_b64 s[2:3], vcc
	s_xor_b64 s[2:3], exec, s[2:3]
	s_cbranch_execz .LBB0_1446
	s_add_i32 s78, s20, 0x900
	s_lshl_b64 s[4:5], s[78:79], 2
	s_add_u32 s8, s82, s4
	s_addc_u32 s9, s83, s5
	s_waitcnt lgkmcnt(0)
	global_load_dword v0, v65, s[8:9] sc1
	s_waitcnt vmcnt(0)
	v_cmp_eq_u32_e32 vcc, v0, v1
	s_and_saveexec_b64 s[4:5], vcc
	s_cbranch_execz .LBB0_1445
	s_mov_b32 s21, 1
	s_mov_b64 s[10:11], 0
	s_branch .LBB0_1436

.LBB0_1449:
	s_or_b64 exec, exec, s[4:5]
	s_waitcnt vmcnt(0)
	v_readfirstlane_b32 s2, v2
	v_cvt_f32_u32_e32 v2, v0
	v_sub_u32_e32 v3, 0, v0
	v_add_u32_e32 v1, s2, v1
	v_readlane_b32 s2, v243, 39
	v_rcp_iflag_f32_e32 v2, v2
	v_readlane_b32 s3, v243, 40
	s_mov_b64 s[4:5], -1
	v_mul_f32_e32 v2, 0x4f7ffffe, v2
	v_cvt_u32_f32_e32 v2, v2
	v_mul_lo_u32 v3, v3, v2
	v_mul_hi_u32 v3, v2, v3
	v_add_u32_e32 v2, v2, v3
	v_mul_hi_u32 v2, v1, v2
	v_mul_lo_u32 v3, v2, v0
	v_sub_u32_e32 v3, v1, v3
	v_cmp_ge_u32_e32 vcc, v3, v0
	v_add_u32_e32 v4, 1, v2
	v_add_u32_e32 v1, 1, v1
	v_cndmask_b32_e32 v2, v2, v4, vcc
	v_sub_u32_e32 v4, v3, v0
	v_cndmask_b32_e32 v3, v3, v4, vcc
	v_cmp_ge_u32_e32 vcc, v3, v0
	v_add_u32_e32 v3, 1, v2
	s_nop 0
	v_cndmask_b32_e32 v2, v2, v3, vcc
	v_mul_lo_u32 v3, v0, v2
	v_add_u32_e32 v0, v3, v0
	v_cmp_ne_u32_e32 vcc, v1, v0
	v_mov_b64_e32 v[0:1], s[2:3]
	s_mov_b32 s100, 1
	s_and_saveexec_b64 s[2:3], vcc
	s_cbranch_execz .LBB0_1461
	s_mov_b32 s100, 0
	s_add_i32 s78, s20, 0x900
	s_lshl_b64 s[4:5], s[78:79], 2
	s_add_u32 s4, s82, s4
	s_addc_u32 s5, s83, s5
	s_mov_b64 s[8:9], 0
	s_nop 3
	global_load_dword v0, v65, s[4:5] sc1
	s_waitcnt vmcnt(0)
	v_mov_b32_e32 v2, s101
	v_cmp_eq_u32_e32 vcc, v0, v2
	s_and_saveexec_b64 s[4:5], vcc
	s_cbranch_execz .LBB0_1460
	s_mov_b32 s18, 1
	s_branch .LBB0_1453

.LBB0_1455:
	s_add_i32 s78, s20, 0x900
	s_lshl_b64 s[12:13], s[78:79], 2
	s_add_u32 s12, s82, s12
	s_addc_u32 s13, s83, s13
	s_add_i32 s18, s18, 1
	s_mov_b64 s[14:15], -1
	s_nop 2
	global_load_dword v0, v65, s[12:13] sc1
	s_waitcnt vmcnt(0)
	v_cmp_ne_u32_e32 vcc, v0, v2
	s_orn2_b64 s[12:13], vcc, exec
	s_branch .LBB0_1452

.LBB0_1463:
	s_or_b64 exec, exec, s[2:3]
	s_mov_b64 s[2:3], exec
	v_mbcnt_lo_u32_b32 v0, s2, 0
	v_mbcnt_hi_u32_b32 v0, s3, v0
	v_cmp_eq_u32_e32 vcc, 0, v0
	s_waitcnt vmcnt(0)
	s_and_saveexec_b64 s[4:5], vcc
	s_cbranch_execz .LBB0_1465
	s_cmp_eq_u32 s100, 0
	s_cbranch_scc1 .Lxb_relskip_8
	s_add_u32 s8, s82, 0x2400
	s_addc_u32 s9, s83, 0
	s_bcnt1_i32_b64 s2, s[2:3]
	v_mov_b32_e32 v0, s2
	global_atomic_add v65, v0, s[8:9]
	global_atomic_add v65, v0, s[8:9] offset:256
	global_atomic_add v65, v0, s[8:9] offset:512
	global_atomic_add v65, v0, s[8:9] offset:768
	global_atomic_add v65, v0, s[8:9] offset:1024
	global_atomic_add v65, v0, s[8:9] offset:1280
	global_atomic_add v65, v0, s[8:9] offset:1536
	global_atomic_add v65, v0, s[8:9] offset:1792
	global_atomic_add v65, v0, s[8:9] offset:2048
	global_atomic_add v65, v0, s[8:9] offset:2304
	global_atomic_add v65, v0, s[8:9] offset:2560
	global_atomic_add v65, v0, s[8:9] offset:2816
	global_atomic_add v65, v0, s[8:9] offset:3072
	global_atomic_add v65, v0, s[8:9] offset:3328
	global_atomic_add v65, v0, s[8:9] offset:3584
	global_atomic_add v65, v0, s[8:9] offset:3840

.LBB0_1565:
	s_cmp_eq_u32 s100, 0
	s_cbranch_scc1 .Lxb_relskip_9
	s_add_u32 s6, s82, 0x2400
	s_addc_u32 s7, s83, 0
	s_bcnt1_i32_b64 s2, s[2:3]
	v_mov_b32_e32 v0, s2
	global_atomic_add v65, v0, s[6:7]
	global_atomic_add v65, v0, s[6:7] offset:256
	global_atomic_add v65, v0, s[6:7] offset:512
	global_atomic_add v65, v0, s[6:7] offset:768
	global_atomic_add v65, v0, s[6:7] offset:1024
	global_atomic_add v65, v0, s[6:7] offset:1280
	global_atomic_add v65, v0, s[6:7] offset:1536
	global_atomic_add v65, v0, s[6:7] offset:1792
	global_atomic_add v65, v0, s[6:7] offset:2048
	global_atomic_add v65, v0, s[6:7] offset:2304
	global_atomic_add v65, v0, s[6:7] offset:2560
	global_atomic_add v65, v0, s[6:7] offset:2816
	global_atomic_add v65, v0, s[6:7] offset:3072
	global_atomic_add v65, v0, s[6:7] offset:3328
	global_atomic_add v65, v0, s[6:7] offset:3584
	global_atomic_add v65, v0, s[6:7] offset:3840
.Lxb_relskip_9:
	s_getpc_b64 s[98:99]
